# grid barrier: last global arriver bumps all XCD release words directly (one hop less) on top of version B
# speedup vs baseline: 1.0064x; 1.0064x over previous
; __device__ __forceinline__ unsigned xb_ld(unsigned* p)              { return __hip_atomic_load(p, __ATOMIC_RELAXED, __HIP_MEMORY_SCOPE_AGENT); }
; __device__ __forceinline__ unsigned xb_add(unsigned* p, unsigned v) { return __hip_atomic_fetch_add(p, v, __ATOMIC_RELAXED, __HIP_MEMORY_SCOPE_AGENT); }
; #define XB_SPIN(cond, bar) do { unsigned _sp = 0; while (cond) { __builtin_amdgcn_s_sleep(1); \
;     if ((++_sp & 255u) == 0u) { if (xb_ld(&(bar)[XB_TMO])) break; if (_sp > XB_SPIN_CAP) { atomicAdd(&(bar)[XB_TMO], 1u); break; } } } } while (0)
; __device__ __forceinline__ void xcd_barrier(const XcdBarrier& b) {
;     ...
;         if (old + 1u == (gen + 1u) * nloc) {
;             __builtin_amdgcn_fence(__ATOMIC_RELEASE, "agent");
;             asm volatile("s_waitcnt vmcnt(0)" ::: "memory");
;             const unsigned og = xb_add(&bar[XB_TOP], 1u);
;             const unsigned tg = og / nx;
;             if (og + 1u == (tg + 1u) * nx) xb_add(&bar[XB_TOPGEN], 1u);
;             else XB_SPIN(xb_ld(&bar[XB_TOPGEN]) == tg, bar);
;             __builtin_amdgcn_fence(__ATOMIC_ACQUIRE, "agent");
;             xb_add(&bar[XB_XGEN(b.x)], 1u);
;             asm volatile("s_waitcnt vmcnt(0)" ::: "memory");
.LBB0_86:
	s_or_b64 exec, exec, s[4:5]
	s_and_saveexec_b64 s[4:5], s[8:9]
	s_cbranch_execz .LBB0_88
	v_mov_b32_e32 v1, 1
	global_atomic_add v[2:3], v1, off
	v_mov_b32_e32 v5, 0x6400
	global_atomic_add v5, v1, s[76:77]
	global_atomic_add v5, v1, s[76:77] offset:256
	global_atomic_add v5, v1, s[76:77] offset:512
	global_atomic_add v5, v1, s[76:77] offset:768
	global_atomic_add v5, v1, s[76:77] offset:1024
	global_atomic_add v5, v1, s[76:77] offset:1280
	global_atomic_add v5, v1, s[76:77] offset:1536
	global_atomic_add v5, v1, s[76:77] offset:1792
	global_atomic_add v5, v1, s[76:77] offset:2048
	global_atomic_add v5, v1, s[76:77] offset:2304
	global_atomic_add v5, v1, s[76:77] offset:2560
	global_atomic_add v5, v1, s[76:77] offset:2816
	global_atomic_add v5, v1, s[76:77] offset:3072
	global_atomic_add v5, v1, s[76:77] offset:3328
	global_atomic_add v5, v1, s[76:77] offset:3584
	global_atomic_add v5, v1, s[76:77] offset:3840
.LBB0_88:
	s_or_b64 exec, exec, s[4:5]
	s_mov_b64 s[4:5], exec
	v_mbcnt_lo_u32_b32 v1, s4, 0
	v_mbcnt_hi_u32_b32 v1, s5, v1
	v_cmp_eq_u32_e32 vcc, 0, v1
	s_waitcnt vmcnt(0)
	buffer_inv sc1
	s_and_saveexec_b64 s[6:7], vcc
	s_cbranch_execz .LBB0_90
	s_bcnt1_i32_b64 s4, s[4:5]
	v_mov_b32_e32 v1, 0x2000
	v_mov_b32_e32 v2, s4
	s_nop 0
